# v23
# speedup vs baseline: 1.0159x; 1.0089x over previous
.LBB1_3:
	s_waitcnt lgkmcnt(0)
	s_cmp_lg_u32 s31, 1
	s_cbranch_scc1 .Lk1_noprio
	s_setprio 1

.LBB1_12:
	s_waitcnt vmcnt(8)
	s_waitcnt lgkmcnt(0)
	s_barrier
	s_waitcnt lgkmcnt(0)
	v_mfma_f32_16x16x32_f16 v[128:131], v[148:151], v[166:169], v[128:131]
	v_mfma_f32_16x16x32_f16 v[128:131], v[152:155], v[174:177], v[128:131]
	v_mfma_f32_16x16x32_f16 v[120:123], v[160:163], v[174:177], v[120:123]
	v_mfma_f32_16x16x32_f16 v[120:123], v[156:159], v[166:169], v[120:123]
	v_mfma_f32_16x16x32_f16 v[104:107], v[156:159], v[170:173], v[104:107]
	v_mfma_f32_16x16x32_f16 v[104:107], v[160:163], v[178:181], v[104:107]
	v_mfma_f32_16x16x32_f16 v[112:115], v[152:155], v[178:181], v[112:115]
	v_mfma_f32_16x16x32_f16 v[112:115], v[148:151], v[170:173], v[112:115]
	v_mfma_f32_16x16x32_f16 v[96:99], v[148:151], v[182:185], v[96:99]
	v_mfma_f32_16x16x32_f16 v[96:99], v[152:155], v[190:193], v[96:99]
	v_mfma_f32_16x16x32_f16 v[88:91], v[160:163], v[190:193], v[88:91]
	v_mfma_f32_16x16x32_f16 v[88:91], v[156:159], v[182:185], v[88:91]
	v_mfma_f32_16x16x32_f16 v[72:75], v[156:159], v[186:189], v[72:75]
	v_mfma_f32_16x16x32_f16 v[72:75], v[160:163], v[214:217], v[72:75]
	v_mfma_f32_16x16x32_f16 v[80:83], v[152:155], v[214:217], v[80:83]
	v_mfma_f32_16x16x32_f16 v[80:83], v[148:151], v[186:189], v[80:83]
	v_mfma_f32_16x16x32_f16 v[124:127], v[132:135], v[166:169], v[124:127]
	v_mfma_f32_16x16x32_f16 v[124:127], v[136:139], v[174:177], v[124:127]
	v_mfma_f32_16x16x32_f16 v[116:119], v[144:147], v[174:177], v[116:119]
	v_mfma_f32_16x16x32_f16 v[116:119], v[140:143], v[166:169], v[116:119]
	v_mfma_f32_16x16x32_f16 v[100:103], v[140:143], v[170:173], v[100:103]
	v_mfma_f32_16x16x32_f16 v[100:103], v[144:147], v[178:181], v[100:103]
	v_mfma_f32_16x16x32_f16 v[108:111], v[136:139], v[178:181], v[108:111]
	v_mfma_f32_16x16x32_f16 v[108:111], v[132:135], v[170:173], v[108:111]
	v_mfma_f32_16x16x32_f16 v[92:95], v[132:135], v[182:185], v[92:95]
	v_mfma_f32_16x16x32_f16 v[92:95], v[136:139], v[190:193], v[92:95]
	v_mfma_f32_16x16x32_f16 v[84:87], v[144:147], v[190:193], v[84:87]
	v_mfma_f32_16x16x32_f16 v[84:87], v[140:143], v[182:185], v[84:87]
	v_mfma_f32_16x16x32_f16 v[68:71], v[140:143], v[186:189], v[68:71]
	v_mfma_f32_16x16x32_f16 v[68:71], v[144:147], v[214:217], v[68:71]
	v_mfma_f32_16x16x32_f16 v[76:79], v[136:139], v[214:217], v[76:79]
	v_mfma_f32_16x16x32_f16 v[76:79], v[132:135], v[186:189], v[76:79]
	s_barrier
	s_andn2_b64 vcc, exec, s[4:5]
	s_cbranch_vccnz .LBB1_16
	v_cvt_pkrtz_f16_f32 v166, v0, v1
	v_cvt_pkrtz_f16_f32 v167, v2, v3
	v_add_u32_e32 v166, 0x20002, v166
	v_add_u32_e32 v167, 0x20002, v167
	v_and_b32_e32 v166, 0xfffcfffc, v166
	v_and_b32_e32 v167, 0xfffcfffc, v167
	global_store_dwordx2 v231, v[166:167], s[90:91]

.LBB1_20:
	s_waitcnt lgkmcnt(0)
	s_barrier
	s_waitcnt lgkmcnt(0)
	v_mfma_f32_16x16x32_f16 v[64:67], v[148:151], v[188:191], v[64:67]
	v_mfma_f32_16x16x32_f16 v[64:67], v[152:155], v[192:195], v[64:67]
	v_mfma_f32_16x16x32_f16 v[56:59], v[160:163], v[192:195], v[56:59]
	v_mfma_f32_16x16x32_f16 v[56:59], v[156:159], v[188:191], v[56:59]
	v_mfma_f32_16x16x32_f16 v[40:43], v[156:159], v[176:179], v[40:43]
	v_mfma_f32_16x16x32_f16 v[40:43], v[160:163], v[180:183], v[40:43]
	v_mfma_f32_16x16x32_f16 v[48:51], v[152:155], v[180:183], v[48:51]
	v_mfma_f32_16x16x32_f16 v[48:51], v[148:151], v[176:179], v[48:51]
	v_mfma_f32_16x16x32_f16 v[32:35], v[148:151], v[172:175], v[32:35]
	v_mfma_f32_16x16x32_f16 v[32:35], v[152:155], v[184:187], v[32:35]
	v_mfma_f32_16x16x32_f16 v[24:27], v[160:163], v[184:187], v[24:27]
	v_mfma_f32_16x16x32_f16 v[24:27], v[156:159], v[172:175], v[24:27]
	v_mfma_f32_16x16x32_f16 v[8:11], v[156:159], v[164:167], v[8:11]
	v_mfma_f32_16x16x32_f16 v[8:11], v[160:163], v[168:171], v[8:11]
	v_mfma_f32_16x16x32_f16 v[16:19], v[152:155], v[168:171], v[16:19]
	v_mfma_f32_16x16x32_f16 v[16:19], v[148:151], v[164:167], v[16:19]
	v_mfma_f32_16x16x32_f16 v[60:63], v[132:135], v[188:191], v[60:63]
	v_mfma_f32_16x16x32_f16 v[60:63], v[136:139], v[192:195], v[60:63]
	v_mfma_f32_16x16x32_f16 v[52:55], v[144:147], v[192:195], v[52:55]
	v_mfma_f32_16x16x32_f16 v[52:55], v[140:143], v[188:191], v[52:55]
	v_mfma_f32_16x16x32_f16 v[36:39], v[140:143], v[176:179], v[36:39]
	v_mfma_f32_16x16x32_f16 v[36:39], v[144:147], v[180:183], v[36:39]
	v_mfma_f32_16x16x32_f16 v[44:47], v[136:139], v[180:183], v[44:47]
	v_mfma_f32_16x16x32_f16 v[44:47], v[132:135], v[176:179], v[44:47]
	v_mfma_f32_16x16x32_f16 v[28:31], v[132:135], v[172:175], v[28:31]
	v_mfma_f32_16x16x32_f16 v[28:31], v[136:139], v[184:187], v[28:31]
	v_mfma_f32_16x16x32_f16 v[20:23], v[144:147], v[184:187], v[20:23]
	v_mfma_f32_16x16x32_f16 v[20:23], v[140:143], v[172:175], v[20:23]
	v_mfma_f32_16x16x32_f16 v[4:7], v[140:143], v[164:167], v[4:7]
	v_mfma_f32_16x16x32_f16 v[4:7], v[144:147], v[168:171], v[4:7]
	v_mfma_f32_16x16x32_f16 v[12:15], v[136:139], v[168:171], v[12:15]
	v_mfma_f32_16x16x32_f16 v[12:15], v[132:135], v[164:167], v[12:15]
	s_barrier
	s_add_u32 s48, s48, 0x100000
	ds_read_b128 v[148:151], v228 offset:32768
	ds_read_b128 v[152:155], v229 offset:32768
	s_addc_u32 s49, s49, 0
	s_mov_b32 m0, s57
	ds_read_b128 v[156:159], v228 offset:34816
	ds_read_b128 v[160:163], v229 offset:34816
	ds_read_b128 v[132:135], v228 offset:49152
	ds_read_b128 v[136:139], v229 offset:49152
	ds_read_b128 v[140:143], v228 offset:51200
	ds_read_b128 v[144:147], v229 offset:51200
	ds_read_b128 v[188:191], v226 offset:32768
	ds_read_b128 v[176:179], v226 offset:34816
	ds_read_b128 v[192:195], v227 offset:32768
	ds_read_b128 v[180:183], v227 offset:34816
	ds_read_b128 v[172:175], v226 offset:36864
	ds_read_b128 v[164:167], v226 offset:38912
	ds_read_b128 v[184:187], v227 offset:36864
	ds_read_b128 v[168:171], v227 offset:38912
	global_load_lds_dwordx4 v202, s[48:49]
	s_mov_b32 m0, s58
	s_nop 0
	global_load_lds_dwordx4 v198, s[48:49]
	s_mov_b64 s[48:49], -1
	s_mov_b64 vcc, s[4:5]
	s_cbranch_vccz .LBB1_22
	s_waitcnt vmcnt(8)
	s_mov_b64 s[48:49], 0

.LBB1_24:
	s_waitcnt lgkmcnt(0)
	s_barrier
	s_waitcnt lgkmcnt(0)
	v_mfma_f32_16x16x32_f16 v[128:131], v[148:151], v[188:191], v[128:131]
	v_mfma_f32_16x16x32_f16 v[128:131], v[152:155], v[192:195], v[128:131]
	v_mfma_f32_16x16x32_f16 v[120:123], v[160:163], v[192:195], v[120:123]
	v_mfma_f32_16x16x32_f16 v[120:123], v[156:159], v[188:191], v[120:123]
	v_mfma_f32_16x16x32_f16 v[104:107], v[156:159], v[176:179], v[104:107]
	v_mfma_f32_16x16x32_f16 v[104:107], v[160:163], v[180:183], v[104:107]
	v_mfma_f32_16x16x32_f16 v[112:115], v[152:155], v[180:183], v[112:115]
	v_mfma_f32_16x16x32_f16 v[112:115], v[148:151], v[176:179], v[112:115]
	v_mfma_f32_16x16x32_f16 v[96:99], v[148:151], v[172:175], v[96:99]
	v_mfma_f32_16x16x32_f16 v[96:99], v[152:155], v[184:187], v[96:99]
	v_mfma_f32_16x16x32_f16 v[88:91], v[160:163], v[184:187], v[88:91]
	v_mfma_f32_16x16x32_f16 v[88:91], v[156:159], v[172:175], v[88:91]
	v_mfma_f32_16x16x32_f16 v[72:75], v[156:159], v[164:167], v[72:75]
	v_mfma_f32_16x16x32_f16 v[72:75], v[160:163], v[168:171], v[72:75]
	v_mfma_f32_16x16x32_f16 v[80:83], v[152:155], v[168:171], v[80:83]
	v_mfma_f32_16x16x32_f16 v[80:83], v[148:151], v[164:167], v[80:83]
	v_mfma_f32_16x16x32_f16 v[124:127], v[132:135], v[188:191], v[124:127]
	v_mfma_f32_16x16x32_f16 v[124:127], v[136:139], v[192:195], v[124:127]
	v_mfma_f32_16x16x32_f16 v[116:119], v[144:147], v[192:195], v[116:119]
	v_mfma_f32_16x16x32_f16 v[116:119], v[140:143], v[188:191], v[116:119]
	v_mfma_f32_16x16x32_f16 v[100:103], v[140:143], v[176:179], v[100:103]
	v_mfma_f32_16x16x32_f16 v[100:103], v[144:147], v[180:183], v[100:103]
	v_mfma_f32_16x16x32_f16 v[108:111], v[136:139], v[180:183], v[108:111]
	v_mfma_f32_16x16x32_f16 v[108:111], v[132:135], v[176:179], v[108:111]
	v_mfma_f32_16x16x32_f16 v[92:95], v[132:135], v[172:175], v[92:95]
	v_mfma_f32_16x16x32_f16 v[92:95], v[136:139], v[184:187], v[92:95]
	v_mfma_f32_16x16x32_f16 v[84:87], v[144:147], v[184:187], v[84:87]
	v_mfma_f32_16x16x32_f16 v[84:87], v[140:143], v[172:175], v[84:87]
	v_mfma_f32_16x16x32_f16 v[68:71], v[140:143], v[164:167], v[68:71]
	v_mfma_f32_16x16x32_f16 v[68:71], v[144:147], v[168:171], v[68:71]
	v_mfma_f32_16x16x32_f16 v[76:79], v[136:139], v[168:171], v[76:79]
	v_mfma_f32_16x16x32_f16 v[76:79], v[132:135], v[164:167], v[76:79]
	s_barrier
	s_mov_b32 m0, s59
	s_add_u32 s4, s46, 0x100080
	ds_read_b128 v[164:167], v226 offset:49152
	ds_read_b128 v[168:171], v226 offset:51200
	ds_read_b128 v[172:175], v227 offset:49152
	ds_read_b128 v[176:179], v227 offset:51200
	ds_read_b128 v[180:183], v226 offset:53248
	ds_read_b128 v[184:187], v226 offset:55296
	ds_read_b128 v[188:191], v227 offset:53248
	ds_read_b128 v[192:195], v227 offset:55296
	global_load_lds_dwordx4 v200, s[84:85]
	s_mov_b32 m0, s60
	s_addc_u32 s5, s47, 0
	global_load_lds_dwordx4 v196, s[84:85]
	s_mov_b32 m0, s63
	s_nop 0
	global_load_lds_dwordx4 v200, s[4:5]
	s_mov_b32 m0, s64
	s_nop 0
	global_load_lds_dwordx4 v196, s[4:5]
	s_mov_b32 m0, s61
	s_nop 0
	global_load_lds_dwordx4 v202, s[86:87]
	s_mov_b32 m0, s62
	s_nop 0
	global_load_lds_dwordx4 v198, s[86:87]
	s_waitcnt vmcnt(8)
	s_waitcnt lgkmcnt(0)
	s_barrier
	s_waitcnt lgkmcnt(0)
	v_mfma_f32_16x16x32_f16 v[64:67], v[148:151], v[164:167], v[64:67]
	v_mfma_f32_16x16x32_f16 v[64:67], v[152:155], v[172:175], v[64:67]
	v_mfma_f32_16x16x32_f16 v[56:59], v[160:163], v[172:175], v[56:59]
	v_mfma_f32_16x16x32_f16 v[56:59], v[156:159], v[164:167], v[56:59]
	v_mfma_f32_16x16x32_f16 v[40:43], v[156:159], v[168:171], v[40:43]
	v_mfma_f32_16x16x32_f16 v[40:43], v[160:163], v[176:179], v[40:43]
	v_mfma_f32_16x16x32_f16 v[48:51], v[152:155], v[176:179], v[48:51]
	v_mfma_f32_16x16x32_f16 v[48:51], v[148:151], v[168:171], v[48:51]
	v_mfma_f32_16x16x32_f16 v[32:35], v[148:151], v[180:183], v[32:35]
	v_mfma_f32_16x16x32_f16 v[32:35], v[152:155], v[188:191], v[32:35]
	v_mfma_f32_16x16x32_f16 v[24:27], v[160:163], v[188:191], v[24:27]
	v_mfma_f32_16x16x32_f16 v[24:27], v[156:159], v[180:183], v[24:27]
	v_mfma_f32_16x16x32_f16 v[8:11], v[156:159], v[184:187], v[8:11]
	v_mfma_f32_16x16x32_f16 v[8:11], v[160:163], v[192:195], v[8:11]
	v_mfma_f32_16x16x32_f16 v[16:19], v[152:155], v[192:195], v[16:19]
	v_mfma_f32_16x16x32_f16 v[16:19], v[148:151], v[184:187], v[16:19]
	v_mfma_f32_16x16x32_f16 v[60:63], v[132:135], v[164:167], v[60:63]
	v_mfma_f32_16x16x32_f16 v[60:63], v[136:139], v[172:175], v[60:63]
	v_mfma_f32_16x16x32_f16 v[52:55], v[144:147], v[172:175], v[52:55]
	v_mfma_f32_16x16x32_f16 v[52:55], v[140:143], v[164:167], v[52:55]
	v_mfma_f32_16x16x32_f16 v[36:39], v[140:143], v[168:171], v[36:39]
	v_mfma_f32_16x16x32_f16 v[36:39], v[144:147], v[176:179], v[36:39]
	v_mfma_f32_16x16x32_f16 v[44:47], v[136:139], v[176:179], v[44:47]
	v_mfma_f32_16x16x32_f16 v[44:47], v[132:135], v[168:171], v[44:47]
	v_mfma_f32_16x16x32_f16 v[28:31], v[132:135], v[180:183], v[28:31]
	v_mfma_f32_16x16x32_f16 v[28:31], v[136:139], v[188:191], v[28:31]
	v_mfma_f32_16x16x32_f16 v[20:23], v[144:147], v[188:191], v[20:23]
	v_mfma_f32_16x16x32_f16 v[20:23], v[140:143], v[180:183], v[20:23]
	v_mfma_f32_16x16x32_f16 v[4:7], v[140:143], v[184:187], v[4:7]
	v_mfma_f32_16x16x32_f16 v[4:7], v[144:147], v[192:195], v[4:7]
	v_mfma_f32_16x16x32_f16 v[12:15], v[136:139], v[192:195], v[12:15]
	v_mfma_f32_16x16x32_f16 v[12:15], v[132:135], v[184:187], v[12:15]
	s_barrier
	s_add_u32 s80, s80, 0x100
	s_addc_u32 s81, s81, 0
	s_add_u32 s44, s44, 0x100
	s_addc_u32 s45, s45, 0
	s_cmp_gt_u32 s82, 61
	s_cbranch_scc1 .LBB1_4
	s_mov_b32 s48, s82
	s_branch .LBB1_9

.LBB2_7:
	s_cmp_lg_u32 s16, 1
	s_cbranch_scc1 .Lk2_noprio
	s_setprio 1

.LBB2_20:
	s_add_u32 s30, s28, 0xffc80080
	s_addc_u32 s31, s29, -1
	s_cmpk_eq_i32 s58, 0xdc
	s_cselect_b32 s35, s25, s31
	s_cselect_b32 s34, s24, s30
	s_cselect_b32 s31, s27, s57
	s_cselect_b32 s30, s26, s56
	s_add_i32 m0, s37, 0xc000
	ds_read_b128 v[166:169], v143
	ds_read_b128 v[170:173], v147
	ds_read_b128 v[174:177], v149
	ds_read_b128 v[178:181], v150
	ds_read_b128 v[182:185], v151
	ds_read_b128 v[186:189], v152
	ds_read_b128 v[190:193], v153
	ds_read_b128 v[194:197], v154
	ds_read_b128 v[198:201], v155
	ds_read_b128 v[202:205], v155 offset:2048
	ds_read_b128 v[206:209], v156
	ds_read_b128 v[210:213], v156 offset:2048
	ds_read_b128 v[214:217], v155 offset:4096
	ds_read_b128 v[218:221], v155 offset:6144
	ds_read_b128 v[222:225], v156 offset:4096
	ds_read_b128 v[226:229], v156 offset:6144
	global_load_lds_dwordx4 v134, s[28:29]
	s_add_i32 m0, s37, 0xe000
	s_nop 0
	global_load_lds_dwordx4 v132, s[28:29]
	s_waitcnt vmcnt(8)
	s_waitcnt lgkmcnt(0)
	s_barrier
	s_waitcnt lgkmcnt(0)
	v_mfma_f32_16x16x32_f16 v[124:127], v[166:169], v[198:201], v[124:127]
	v_mfma_f32_16x16x32_f16 v[124:127], v[170:173], v[206:209], v[124:127]
	v_mfma_f32_16x16x32_f16 v[120:123], v[178:181], v[206:209], v[120:123]
	v_mfma_f32_16x16x32_f16 v[120:123], v[174:177], v[198:201], v[120:123]
	v_mfma_f32_16x16x32_f16 v[112:115], v[174:177], v[202:205], v[112:115]
	v_mfma_f32_16x16x32_f16 v[112:115], v[178:181], v[210:213], v[112:115]
	v_mfma_f32_16x16x32_f16 v[116:119], v[170:173], v[210:213], v[116:119]
	v_mfma_f32_16x16x32_f16 v[116:119], v[166:169], v[202:205], v[116:119]
	v_mfma_f32_16x16x32_f16 v[108:111], v[166:169], v[214:217], v[108:111]
	v_mfma_f32_16x16x32_f16 v[108:111], v[170:173], v[222:225], v[108:111]
	v_mfma_f32_16x16x32_f16 v[100:103], v[178:181], v[222:225], v[100:103]
	v_mfma_f32_16x16x32_f16 v[100:103], v[174:177], v[214:217], v[100:103]
	v_mfma_f32_16x16x32_f16 v[84:87], v[174:177], v[218:221], v[84:87]
	v_mfma_f32_16x16x32_f16 v[84:87], v[178:181], v[226:229], v[84:87]
	v_mfma_f32_16x16x32_f16 v[92:95], v[170:173], v[226:229], v[92:95]
	v_mfma_f32_16x16x32_f16 v[92:95], v[166:169], v[218:221], v[92:95]
	v_mfma_f32_16x16x32_f16 v[104:107], v[182:185], v[198:201], v[104:107]
	v_mfma_f32_16x16x32_f16 v[104:107], v[186:189], v[206:209], v[104:107]
	v_mfma_f32_16x16x32_f16 v[96:99], v[194:197], v[206:209], v[96:99]
	v_mfma_f32_16x16x32_f16 v[96:99], v[190:193], v[198:201], v[96:99]
	v_mfma_f32_16x16x32_f16 v[80:83], v[190:193], v[202:205], v[80:83]
	v_mfma_f32_16x16x32_f16 v[80:83], v[194:197], v[210:213], v[80:83]
	v_mfma_f32_16x16x32_f16 v[88:91], v[186:189], v[210:213], v[88:91]
	v_mfma_f32_16x16x32_f16 v[88:91], v[182:185], v[202:205], v[88:91]
	v_mfma_f32_16x16x32_f16 v[76:79], v[182:185], v[214:217], v[76:79]
	v_mfma_f32_16x16x32_f16 v[76:79], v[186:189], v[222:225], v[76:79]
	v_mfma_f32_16x16x32_f16 v[72:75], v[194:197], v[222:225], v[72:75]
	v_mfma_f32_16x16x32_f16 v[72:75], v[190:193], v[214:217], v[72:75]
	v_mfma_f32_16x16x32_f16 v[64:67], v[190:193], v[218:221], v[64:67]
	v_mfma_f32_16x16x32_f16 v[64:67], v[194:197], v[226:229], v[64:67]
	v_mfma_f32_16x16x32_f16 v[68:71], v[186:189], v[226:229], v[68:71]
	v_mfma_f32_16x16x32_f16 v[68:71], v[182:185], v[218:221], v[68:71]
	s_barrier
	s_add_i32 s59, s43, s36
	s_mov_b32 m0, s59
	ds_read_b128 v[198:201], v155 offset:16384
	ds_read_b128 v[202:205], v155 offset:18432
	ds_read_b128 v[206:209], v156 offset:16384
	ds_read_b128 v[210:213], v156 offset:18432
	ds_read_b128 v[214:217], v155 offset:20480
	ds_read_b128 v[218:221], v155 offset:22528
	ds_read_b128 v[222:225], v156 offset:20480
	ds_read_b128 v[226:229], v156 offset:22528
	global_load_lds_dwordx4 v128, s[30:31]
	s_add_i32 m0, s59, 0x2000
	s_add_u32 s60, s30, 0x380000
	s_addc_u32 s61, s31, 0
	s_add_i32 s59, s44, s36
	global_load_lds_dwordx4 v130, s[30:31]
	s_mov_b32 m0, s59
	s_add_u32 s62, s30, 0x80
	s_addc_u32 s63, s31, 0
	global_load_lds_dwordx4 v128, s[60:61]
	s_add_i32 m0, s59, 0x2000
	s_add_u32 s64, s34, 0x80
	s_addc_u32 s65, s35, 0
	global_load_lds_dwordx4 v130, s[60:61]
	s_mov_b32 m0, s37
	s_nop 0
	global_load_lds_dwordx4 v128, s[34:35]
	s_mov_b32 m0, s38
	s_nop 0
	global_load_lds_dwordx4 v130, s[34:35]
	s_waitcnt vmcnt(8)
	s_waitcnt lgkmcnt(0)
	s_barrier
	s_waitcnt lgkmcnt(0)
	v_mfma_f32_16x16x32_f16 v[60:63], v[166:169], v[198:201], v[60:63]
	v_mfma_f32_16x16x32_f16 v[60:63], v[170:173], v[206:209], v[60:63]
	v_mfma_f32_16x16x32_f16 v[56:59], v[178:181], v[206:209], v[56:59]
	v_mfma_f32_16x16x32_f16 v[56:59], v[174:177], v[198:201], v[56:59]
	v_mfma_f32_16x16x32_f16 v[48:51], v[174:177], v[202:205], v[48:51]
	v_mfma_f32_16x16x32_f16 v[48:51], v[178:181], v[210:213], v[48:51]
	v_mfma_f32_16x16x32_f16 v[52:55], v[170:173], v[210:213], v[52:55]
	v_mfma_f32_16x16x32_f16 v[52:55], v[166:169], v[202:205], v[52:55]
	v_mfma_f32_16x16x32_f16 v[40:43], v[166:169], v[214:217], v[40:43]
	v_mfma_f32_16x16x32_f16 v[40:43], v[170:173], v[222:225], v[40:43]
	v_mfma_f32_16x16x32_f16 v[32:35], v[178:181], v[222:225], v[32:35]
	v_mfma_f32_16x16x32_f16 v[32:35], v[174:177], v[214:217], v[32:35]
	v_mfma_f32_16x16x32_f16 v[8:11], v[174:177], v[218:221], v[8:11]
	v_mfma_f32_16x16x32_f16 v[8:11], v[178:181], v[226:229], v[8:11]
	v_mfma_f32_16x16x32_f16 v[12:15], v[170:173], v[226:229], v[12:15]
	v_mfma_f32_16x16x32_f16 v[12:15], v[166:169], v[218:221], v[12:15]
	v_mfma_f32_16x16x32_f16 v[44:47], v[182:185], v[198:201], v[44:47]
	v_mfma_f32_16x16x32_f16 v[44:47], v[186:189], v[206:209], v[44:47]
	v_mfma_f32_16x16x32_f16 v[36:39], v[194:197], v[206:209], v[36:39]
	v_mfma_f32_16x16x32_f16 v[36:39], v[190:193], v[198:201], v[36:39]
	v_mfma_f32_16x16x32_f16 v[24:27], v[190:193], v[202:205], v[24:27]
	v_mfma_f32_16x16x32_f16 v[24:27], v[194:197], v[210:213], v[24:27]
	v_mfma_f32_16x16x32_f16 v[28:31], v[186:189], v[210:213], v[28:31]
	v_mfma_f32_16x16x32_f16 v[28:31], v[182:185], v[202:205], v[28:31]
	v_mfma_f32_16x16x32_f16 v[20:23], v[182:185], v[214:217], v[20:23]
	v_mfma_f32_16x16x32_f16 v[20:23], v[186:189], v[222:225], v[20:23]
	v_mfma_f32_16x16x32_f16 v[16:19], v[194:197], v[222:225], v[16:19]
	v_mfma_f32_16x16x32_f16 v[16:19], v[190:193], v[214:217], v[16:19]
	v_mfma_f32_16x16x32_f16 v[0:3], v[190:193], v[218:221], v[0:3]
	v_mfma_f32_16x16x32_f16 v[0:3], v[194:197], v[226:229], v[0:3]
	v_mfma_f32_16x16x32_f16 v[4:7], v[186:189], v[226:229], v[4:7]
	v_mfma_f32_16x16x32_f16 v[4:7], v[182:185], v[218:221], v[4:7]
	s_barrier
	s_add_u32 s34, s34, 0x380000
	s_addc_u32 s35, s35, 0
	s_mov_b32 m0, s39
	ds_read_b128 v[166:169], v157
	ds_read_b128 v[170:173], v158
	ds_read_b128 v[174:177], v159
	ds_read_b128 v[178:181], v160
	ds_read_b128 v[182:185], v161
	ds_read_b128 v[186:189], v162
	ds_read_b128 v[190:193], v163
	ds_read_b128 v[194:197], v164
	ds_read_b128 v[198:201], v155 offset:32768
	ds_read_b128 v[202:205], v155 offset:34816
	ds_read_b128 v[206:209], v156 offset:32768
	ds_read_b128 v[210:213], v156 offset:34816
	ds_read_b128 v[214:217], v155 offset:36864
	ds_read_b128 v[218:221], v155 offset:38912
	ds_read_b128 v[222:225], v156 offset:36864
	ds_read_b128 v[226:229], v156 offset:38912
	global_load_lds_dwordx4 v128, s[34:35]
	s_mov_b32 m0, s40
	s_nop 0
	global_load_lds_dwordx4 v130, s[34:35]
	s_waitcnt vmcnt(8)
	s_waitcnt lgkmcnt(0)
	s_barrier
	s_waitcnt lgkmcnt(0)
	v_mfma_f32_16x16x32_f16 v[124:127], v[166:169], v[198:201], v[124:127]
	v_mfma_f32_16x16x32_f16 v[124:127], v[170:173], v[206:209], v[124:127]
	v_mfma_f32_16x16x32_f16 v[120:123], v[178:181], v[206:209], v[120:123]
	v_mfma_f32_16x16x32_f16 v[120:123], v[174:177], v[198:201], v[120:123]
	v_mfma_f32_16x16x32_f16 v[112:115], v[174:177], v[202:205], v[112:115]
	v_mfma_f32_16x16x32_f16 v[112:115], v[178:181], v[210:213], v[112:115]
	v_mfma_f32_16x16x32_f16 v[116:119], v[170:173], v[210:213], v[116:119]
	v_mfma_f32_16x16x32_f16 v[116:119], v[166:169], v[202:205], v[116:119]
	v_mfma_f32_16x16x32_f16 v[108:111], v[166:169], v[214:217], v[108:111]
	v_mfma_f32_16x16x32_f16 v[108:111], v[170:173], v[222:225], v[108:111]
	v_mfma_f32_16x16x32_f16 v[100:103], v[178:181], v[222:225], v[100:103]
	v_mfma_f32_16x16x32_f16 v[100:103], v[174:177], v[214:217], v[100:103]
	v_mfma_f32_16x16x32_f16 v[84:87], v[174:177], v[218:221], v[84:87]
	v_mfma_f32_16x16x32_f16 v[84:87], v[178:181], v[226:229], v[84:87]
	v_mfma_f32_16x16x32_f16 v[92:95], v[170:173], v[226:229], v[92:95]
	v_mfma_f32_16x16x32_f16 v[92:95], v[166:169], v[218:221], v[92:95]
	v_mfma_f32_16x16x32_f16 v[104:107], v[182:185], v[198:201], v[104:107]
	v_mfma_f32_16x16x32_f16 v[104:107], v[186:189], v[206:209], v[104:107]
	v_mfma_f32_16x16x32_f16 v[96:99], v[194:197], v[206:209], v[96:99]
	v_mfma_f32_16x16x32_f16 v[96:99], v[190:193], v[198:201], v[96:99]
	v_mfma_f32_16x16x32_f16 v[80:83], v[190:193], v[202:205], v[80:83]
	v_mfma_f32_16x16x32_f16 v[80:83], v[194:197], v[210:213], v[80:83]
	v_mfma_f32_16x16x32_f16 v[88:91], v[186:189], v[210:213], v[88:91]
	v_mfma_f32_16x16x32_f16 v[88:91], v[182:185], v[202:205], v[88:91]
	v_mfma_f32_16x16x32_f16 v[76:79], v[182:185], v[214:217], v[76:79]
	v_mfma_f32_16x16x32_f16 v[76:79], v[186:189], v[222:225], v[76:79]
	v_mfma_f32_16x16x32_f16 v[72:75], v[194:197], v[222:225], v[72:75]
	v_mfma_f32_16x16x32_f16 v[72:75], v[190:193], v[214:217], v[72:75]
	v_mfma_f32_16x16x32_f16 v[64:67], v[190:193], v[218:221], v[64:67]
	v_mfma_f32_16x16x32_f16 v[64:67], v[194:197], v[226:229], v[64:67]
	v_mfma_f32_16x16x32_f16 v[68:71], v[186:189], v[226:229], v[68:71]
	v_mfma_f32_16x16x32_f16 v[68:71], v[182:185], v[218:221], v[68:71]
	s_barrier
	s_add_i32 s34, s46, s36
	s_mov_b32 m0, s34
	ds_read_b128 v[198:201], v155 offset:49152
	ds_read_b128 v[202:205], v155 offset:51200
	ds_read_b128 v[206:209], v156 offset:49152
	ds_read_b128 v[210:213], v156 offset:51200
	ds_read_b128 v[214:217], v155 offset:53248
	ds_read_b128 v[218:221], v155 offset:55296
	ds_read_b128 v[222:225], v156 offset:53248
	ds_read_b128 v[226:229], v156 offset:55296
	global_load_lds_dwordx4 v128, s[62:63]
	s_add_i32 m0, s34, 0x2000
	s_add_u32 s30, s30, 0x380080
	s_addc_u32 s31, s31, 0
	s_add_i32 s34, s47, s36
	global_load_lds_dwordx4 v130, s[62:63]
	s_mov_b32 m0, s34
	s_nop 0
	global_load_lds_dwordx4 v128, s[30:31]
	s_add_i32 m0, s34, 0x2000
	s_nop 0
	global_load_lds_dwordx4 v130, s[30:31]
	s_mov_b32 m0, s41
	s_nop 0
	global_load_lds_dwordx4 v128, s[64:65]
	s_mov_b32 m0, s42
	s_nop 0
	global_load_lds_dwordx4 v130, s[64:65]
	s_waitcnt vmcnt(8)
	s_waitcnt lgkmcnt(0)
	s_barrier
	s_waitcnt lgkmcnt(0)
	v_mfma_f32_16x16x32_f16 v[60:63], v[166:169], v[198:201], v[60:63]
	v_mfma_f32_16x16x32_f16 v[60:63], v[170:173], v[206:209], v[60:63]
	v_mfma_f32_16x16x32_f16 v[56:59], v[178:181], v[206:209], v[56:59]
	v_mfma_f32_16x16x32_f16 v[56:59], v[174:177], v[198:201], v[56:59]
	v_mfma_f32_16x16x32_f16 v[48:51], v[174:177], v[202:205], v[48:51]
	v_mfma_f32_16x16x32_f16 v[48:51], v[178:181], v[210:213], v[48:51]
	v_mfma_f32_16x16x32_f16 v[52:55], v[170:173], v[210:213], v[52:55]
	v_mfma_f32_16x16x32_f16 v[52:55], v[166:169], v[202:205], v[52:55]
	v_mfma_f32_16x16x32_f16 v[40:43], v[166:169], v[214:217], v[40:43]
	v_mfma_f32_16x16x32_f16 v[40:43], v[170:173], v[222:225], v[40:43]
	v_mfma_f32_16x16x32_f16 v[32:35], v[178:181], v[222:225], v[32:35]
	v_mfma_f32_16x16x32_f16 v[32:35], v[174:177], v[214:217], v[32:35]
	v_mfma_f32_16x16x32_f16 v[8:11], v[174:177], v[218:221], v[8:11]
	v_mfma_f32_16x16x32_f16 v[8:11], v[178:181], v[226:229], v[8:11]
	v_mfma_f32_16x16x32_f16 v[12:15], v[170:173], v[226:229], v[12:15]
	v_mfma_f32_16x16x32_f16 v[12:15], v[166:169], v[218:221], v[12:15]
	v_mfma_f32_16x16x32_f16 v[44:47], v[182:185], v[198:201], v[44:47]
	v_mfma_f32_16x16x32_f16 v[44:47], v[186:189], v[206:209], v[44:47]
	v_mfma_f32_16x16x32_f16 v[36:39], v[194:197], v[206:209], v[36:39]
	v_mfma_f32_16x16x32_f16 v[36:39], v[190:193], v[198:201], v[36:39]
	v_mfma_f32_16x16x32_f16 v[24:27], v[190:193], v[202:205], v[24:27]
	v_mfma_f32_16x16x32_f16 v[24:27], v[194:197], v[210:213], v[24:27]
	v_mfma_f32_16x16x32_f16 v[28:31], v[186:189], v[210:213], v[28:31]
	v_mfma_f32_16x16x32_f16 v[28:31], v[182:185], v[202:205], v[28:31]
	v_mfma_f32_16x16x32_f16 v[20:23], v[182:185], v[214:217], v[20:23]
	v_mfma_f32_16x16x32_f16 v[20:23], v[186:189], v[222:225], v[20:23]
	v_mfma_f32_16x16x32_f16 v[16:19], v[194:197], v[222:225], v[16:19]
	v_mfma_f32_16x16x32_f16 v[16:19], v[190:193], v[214:217], v[16:19]
	v_mfma_f32_16x16x32_f16 v[0:3], v[190:193], v[218:221], v[0:3]
	v_mfma_f32_16x16x32_f16 v[0:3], v[194:197], v[226:229], v[0:3]
	v_mfma_f32_16x16x32_f16 v[4:7], v[186:189], v[226:229], v[4:7]
	v_mfma_f32_16x16x32_f16 v[4:7], v[182:185], v[218:221], v[4:7]
	s_barrier
	s_add_i32 s58, s58, 2
	s_add_u32 s56, s56, 0x100
	s_addc_u32 s57, s57, 0
	s_add_u32 s28, s28, 0x100
	s_addc_u32 s29, s29, 0
	s_cmpk_gt_u32 s58, 0xdd
	s_cbranch_scc0 .LBB2_20
	v_lshl_add_u32 v144, s55, 8, v137
	v_ashrrev_i32_e32 v145, 31, v144
	v_lshl_add_u64 v[138:139], v[144:145], 2, s[10:11]
	global_load_dword v136, v[138:139], off
	global_load_dword v140, v[138:139], off offset:64
	global_load_dword v142, v[138:139], off offset:128
	global_load_dword v146, v[138:139], off offset:192
	global_load_dword v148, v[138:139], off offset:512
	global_load_dword v174, v[138:139], off offset:576
	global_load_dword v176, v[138:139], off offset:640
	s_nop 0
	global_load_dword v138, v[138:139], off offset:704
	v_lshl_or_b32 v166, s54, 8, v141
	v_ashrrev_i32_e32 v167, 31, v166
	v_or_b32_e32 v168, 16, v144
	v_or_b32_e32 v170, 32, v144
	v_or_b32_e32 v172, 48, v144
	v_lshl_add_u64 v[166:167], v[166:167], 2, s[8:9]
	v_lshlrev_b64 v[144:145], 14, v[144:145]
	v_ashrrev_i32_e32 v169, 31, v168
	v_ashrrev_i32_e32 v171, 31, v170
	v_ashrrev_i32_e32 v173, 31, v172
	v_lshl_add_u64 v[144:145], v[166:167], 0, v[144:145]
	v_lshlrev_b64 v[168:169], 14, v[168:169]
	v_lshlrev_b64 v[170:171], 14, v[170:171]
	v_lshlrev_b64 v[172:173], 14, v[172:173]
	v_add_co_u32_e32 v178, vcc, s48, v144
	v_lshl_add_u64 v[168:169], v[166:167], 0, v[168:169]
	v_lshl_add_u64 v[170:171], v[166:167], 0, v[170:171]
	v_lshl_add_u64 v[166:167], v[166:167], 0, v[172:173]
	v_lshl_add_u64 v[172:173], v[144:145], 0, s[16:17]
	v_addc_co_u32_e32 v179, vcc, 0, v145, vcc
	s_mov_b32 s55, s45
	s_mov_b32 s54, s53
	s_mov_b64 s[28:29], s[26:27]
	s_mov_b64 s[30:31], s[24:25]
	s_waitcnt vmcnt(0)
	v_pk_mul_f32 v[126:127], v[136:137], v[126:127] op_sel_hi:[0,1]
	v_pk_mul_f32 v[124:125], v[136:137], v[124:125] op_sel_hi:[0,1]
	v_pk_mul_f32 v[122:123], v[136:137], v[122:123] op_sel_hi:[0,1]
	v_pk_mul_f32 v[120:121], v[136:137], v[120:121] op_sel_hi:[0,1]
	v_pk_mul_f32 v[46:47], v[148:149], v[46:47] op_sel_hi:[0,1]
	v_pk_mul_f32 v[44:45], v[148:149], v[44:45] op_sel_hi:[0,1]
	v_pk_mul_f32 v[106:107], v[136:137], v[106:107] op_sel_hi:[0,1]
	v_pk_mul_f32 v[104:105], v[136:137], v[104:105] op_sel_hi:[0,1]
	v_pk_mul_f32 v[98:99], v[136:137], v[98:99] op_sel_hi:[0,1]
	v_pk_mul_f32 v[96:97], v[136:137], v[96:97] op_sel_hi:[0,1]
	v_pk_mul_f32 v[118:119], v[140:141], v[118:119] op_sel_hi:[0,1]
	v_pk_mul_f32 v[116:117], v[140:141], v[116:117] op_sel_hi:[0,1]
	v_pk_mul_f32 v[114:115], v[140:141], v[114:115] op_sel_hi:[0,1]
	v_pk_mul_f32 v[112:113], v[140:141], v[112:113] op_sel_hi:[0,1]
	v_pk_mul_f32 v[90:91], v[140:141], v[90:91] op_sel_hi:[0,1]
	v_pk_mul_f32 v[88:89], v[140:141], v[88:89] op_sel_hi:[0,1]
	v_pk_mul_f32 v[82:83], v[140:141], v[82:83] op_sel_hi:[0,1]
	v_pk_mul_f32 v[80:81], v[140:141], v[80:81] op_sel_hi:[0,1]
	v_pk_mul_f32 v[110:111], v[142:143], v[110:111] op_sel_hi:[0,1]
	v_pk_mul_f32 v[108:109], v[142:143], v[108:109] op_sel_hi:[0,1]
	v_pk_mul_f32 v[102:103], v[142:143], v[102:103] op_sel_hi:[0,1]
	v_pk_mul_f32 v[100:101], v[142:143], v[100:101] op_sel_hi:[0,1]
	v_pk_mul_f32 v[78:79], v[142:143], v[78:79] op_sel_hi:[0,1]
	v_pk_mul_f32 v[76:77], v[142:143], v[76:77] op_sel_hi:[0,1]
	v_pk_mul_f32 v[74:75], v[142:143], v[74:75] op_sel_hi:[0,1]
	v_pk_mul_f32 v[72:73], v[142:143], v[72:73] op_sel_hi:[0,1]
	v_pk_mul_f32 v[94:95], v[146:147], v[94:95] op_sel_hi:[0,1]
	v_pk_mul_f32 v[92:93], v[146:147], v[92:93] op_sel_hi:[0,1]
	v_pk_mul_f32 v[86:87], v[146:147], v[86:87] op_sel_hi:[0,1]
	v_pk_mul_f32 v[84:85], v[146:147], v[84:85] op_sel_hi:[0,1]
	v_pk_mul_f32 v[70:71], v[146:147], v[70:71] op_sel_hi:[0,1]
	v_pk_mul_f32 v[68:69], v[146:147], v[68:69] op_sel_hi:[0,1]
	v_pk_mul_f32 v[66:67], v[146:147], v[66:67] op_sel_hi:[0,1]
	v_pk_mul_f32 v[64:65], v[146:147], v[64:65] op_sel_hi:[0,1]
	v_pk_mul_f32 v[62:63], v[148:149], v[62:63] op_sel_hi:[0,1]
	v_pk_mul_f32 v[60:61], v[148:149], v[60:61] op_sel_hi:[0,1]
	global_store_dwordx4 v[144:145], v[124:127], off
	global_store_dwordx4 v[144:145], v[120:123], off offset:64
	global_store_dwordx4 v[144:145], v[104:107], off offset:512
	global_store_dwordx4 v[144:145], v[96:99], off offset:576
	global_store_dwordx4 v[168:169], v[116:119], off
	global_store_dwordx4 v[168:169], v[112:115], off offset:64
	global_store_dwordx4 v[168:169], v[88:91], off offset:512
	global_store_dwordx4 v[168:169], v[80:83], off offset:576
	global_store_dwordx4 v[170:171], v[108:111], off
	global_store_dwordx4 v[170:171], v[100:103], off offset:64
	global_store_dwordx4 v[170:171], v[76:79], off offset:512
	global_store_dwordx4 v[170:171], v[72:75], off offset:576
	global_store_dwordx4 v[166:167], v[92:95], off
	global_store_dwordx4 v[166:167], v[84:87], off offset:64
	global_store_dwordx4 v[166:167], v[68:71], off offset:512
	global_store_dwordx4 v[166:167], v[64:67], off offset:576
	global_store_dwordx4 v[178:179], v[60:63], off
	global_store_dwordx4 v[172:173], v[44:47], off offset:512
	v_pk_mul_f32 v[30:31], v[174:175], v[30:31] op_sel_hi:[0,1]
	v_pk_mul_f32 v[28:29], v[174:175], v[28:29] op_sel_hi:[0,1]
	v_add_co_u32_e32 v46, vcc, s49, v144
	v_lshl_add_u64 v[44:45], v[144:145], 0, s[18:19]
	s_nop 0
	v_addc_co_u32_e32 v47, vcc, 0, v145, vcc
	global_store_dwordx4 v[44:45], v[28:31], off offset:512
	v_pk_mul_f32 v[18:19], v[176:177], v[18:19] op_sel_hi:[0,1]
	v_pk_mul_f32 v[16:17], v[176:177], v[16:17] op_sel_hi:[0,1]
	v_add_co_u32_e32 v30, vcc, s50, v144
	v_lshl_add_u64 v[28:29], v[144:145], 0, s[20:21]
	s_nop 0
	v_addc_co_u32_e32 v31, vcc, 0, v145, vcc
	v_pk_mul_f32 v[38:39], v[148:149], v[38:39] op_sel_hi:[0,1]
	v_pk_mul_f32 v[36:37], v[148:149], v[36:37] op_sel_hi:[0,1]
	v_pk_mul_f32 v[26:27], v[174:175], v[26:27] op_sel_hi:[0,1]
	v_pk_mul_f32 v[24:25], v[174:175], v[24:25] op_sel_hi:[0,1]
	global_store_dwordx4 v[28:29], v[16:19], off offset:576
	global_store_dwordx4 v[172:173], v[36:39], off offset:576
	global_store_dwordx4 v[44:45], v[24:27], off offset:576
	v_add_co_u32_e32 v18, vcc, s51, v144
	v_pk_mul_f32 v[38:39], v[174:175], v[54:55] op_sel_hi:[0,1]
	v_pk_mul_f32 v[36:37], v[174:175], v[52:53] op_sel_hi:[0,1]
	v_pk_mul_f32 v[26:27], v[176:177], v[42:43] op_sel_hi:[0,1]
	v_pk_mul_f32 v[24:25], v[176:177], v[40:41] op_sel_hi:[0,1]
	v_addc_co_u32_e32 v19, vcc, 0, v145, vcc
	v_pk_mul_f32 v[58:59], v[148:149], v[58:59] op_sel_hi:[0,1]
	v_pk_mul_f32 v[56:57], v[148:149], v[56:57] op_sel_hi:[0,1]
	global_store_dwordx4 v[46:47], v[36:39], off
	global_store_dwordx4 v[30:31], v[24:27], off
	v_pk_mul_f32 v[22:23], v[176:177], v[22:23] op_sel_hi:[0,1]
	v_pk_mul_f32 v[38:39], v[174:175], v[50:51] op_sel_hi:[0,1]
	v_pk_mul_f32 v[36:37], v[174:175], v[48:49] op_sel_hi:[0,1]
	v_pk_mul_f32 v[26:27], v[176:177], v[34:35] op_sel_hi:[0,1]
	v_pk_mul_f32 v[24:25], v[176:177], v[32:33] op_sel_hi:[0,1]
	v_pk_mul_f32 v[20:21], v[176:177], v[20:21] op_sel_hi:[0,1]
	v_lshl_add_u64 v[16:17], v[144:145], 0, s[22:23]
	v_pk_mul_f32 v[14:15], v[138:139], v[14:15] op_sel_hi:[0,1]
	v_pk_mul_f32 v[12:13], v[138:139], v[12:13] op_sel_hi:[0,1]
	v_pk_mul_f32 v[10:11], v[138:139], v[10:11] op_sel_hi:[0,1]
	v_pk_mul_f32 v[8:9], v[138:139], v[8:9] op_sel_hi:[0,1]
	v_pk_mul_f32 v[6:7], v[138:139], v[6:7] op_sel_hi:[0,1]
	v_pk_mul_f32 v[4:5], v[138:139], v[4:5] op_sel_hi:[0,1]
	v_pk_mul_f32 v[2:3], v[138:139], v[2:3] op_sel_hi:[0,1]
	v_pk_mul_f32 v[0:1], v[138:139], v[0:1] op_sel_hi:[0,1]
	s_mov_b64 vcc, s[0:1]
	global_store_dwordx4 v[172:173], v[56:59], off offset:64
	global_store_dwordx4 v[44:45], v[36:39], off offset:64
	global_store_dwordx4 v[28:29], v[24:27], off offset:64
	global_store_dwordx4 v[28:29], v[20:23], off offset:512
	global_store_dwordx4 v[18:19], v[12:15], off
	global_store_dwordx4 v[16:17], v[8:11], off offset:64
	global_store_dwordx4 v[16:17], v[4:7], off offset:512
	global_store_dwordx4 v[16:17], v[0:3], off offset:576
	s_cbranch_vccz .LBB2_8
	s_waitcnt vmcnt(0)
	s_cmpk_gt_u32 s33, 0xff
	s_cbranch_scc1 .LBB2_24
	s_barrier
